# v50 with spacer lengths A=2 B=1 (x64 cycles) after the sub-head-0 softmax
# speedup vs baseline: 1.0035x; 1.0035x over previous
.LBB0_195:
	v_add_u32_e32 v0, s49, v225
	v_add_u32_e32 v6, v0, v227
	v_add_u32_e32 v7, v0, v228
	ds_read_b128 v[244:247], v6
	ds_read_b128 v[248:251], v6 offset:8192
	ds_read_b128 v[236:239], v7
	ds_read_b128 v[208:211], v7 offset:8192
	v_add_u32_e32 v6, v0, v229
	v_add_u32_e32 v7, v0, v230
	ds_read_b128 v[2:5], v6
	ds_read_b128 v[8:11], v6 offset:8192
	ds_read_b128 v[12:15], v7
	s_xor_b64 s[44:45], s[44:45], -1
	v_add_u32_e32 v6, v0, v226
	s_waitcnt lgkmcnt(6)
	v_mfma_f32_32x32x16_bf16 v[144:159], v[244:247], v[176:179], v[144:159]
	ds_read_b128 v[244:247], v7 offset:8192
	s_waitcnt lgkmcnt(6)
	v_mfma_f32_32x32x16_bf16 v[160:175], v[248:251], v[176:179], v[160:175]
	s_waitcnt lgkmcnt(5)
	v_mfma_f32_32x32x16_bf16 v[144:159], v[236:239], v[180:183], v[144:159]
	ds_read_b128 v[248:251], v6
	ds_read_b128 v[236:239], v6 offset:8192
	s_waitcnt lgkmcnt(6)
	v_mfma_f32_32x32x16_bf16 v[160:175], v[208:211], v[180:183], v[160:175]
	v_add_u32_e32 v7, v0, v231
	s_waitcnt lgkmcnt(5)
	v_mfma_f32_32x32x16_bf16 v[144:159], v[2:5], v[184:187], v[144:159]
	s_waitcnt lgkmcnt(4)
	v_mfma_f32_32x32x16_bf16 v[160:175], v[8:11], v[184:187], v[160:175]
	s_waitcnt lgkmcnt(3)
	v_mfma_f32_32x32x16_bf16 v[144:159], v[12:15], v[188:191], v[144:159]
	s_waitcnt lgkmcnt(2)
	v_mfma_f32_32x32x16_bf16 v[160:175], v[244:247], v[188:191], v[160:175]
	ds_read_b128 v[244:247], v7
	s_nop 9
	v_exp_f32_e32 v6, v144
	v_exp_f32_e32 v3, v145
	v_exp_f32_e32 v10, v148
	v_exp_f32_e32 v11, v149
	v_exp_f32_e32 v12, v150
	v_exp_f32_e32 v148, v152
	v_exp_f32_e32 v150, v153
	v_exp_f32_e32 v156, v156
	v_exp_f32_e32 v157, v157
	v_exp_f32_e32 v5, v146
	v_exp_f32_e32 v152, v154
	v_exp_f32_e32 v158, v158
	v_exp_f32_e32 v8, v147
	v_exp_f32_e32 v13, v151
	v_exp_f32_e32 v154, v155
	v_exp_f32_e32 v159, v159
	v_exp_f32_e32 v2, v160
	v_exp_f32_e32 v144, v164
	v_exp_f32_e32 v149, v168
	v_exp_f32_e32 v160, v172
	v_exp_f32_e32 v4, v161
	v_exp_f32_e32 v145, v165
	v_exp_f32_e32 v151, v169
	v_exp_f32_e32 v161, v173
	v_add_f32_e32 v14, v6, v3
	v_add_f32_e32 v15, v10, v11
	v_add_f32_e32 v164, v148, v150
	v_add_f32_e32 v165, v156, v157
	v_exp_f32_e32 v7, v162
	v_exp_f32_e32 v146, v166
	v_exp_f32_e32 v153, v170
	v_exp_f32_e32 v162, v174
	v_add_f32_e32 v14, v5, v14
	v_add_f32_e32 v15, v12, v15
	v_add_f32_e32 v164, v152, v164
	v_add_f32_e32 v165, v158, v165
	v_exp_f32_e32 v9, v163
	v_exp_f32_e32 v147, v167
	v_exp_f32_e32 v155, v171
	v_exp_f32_e32 v163, v175
	v_add_f32_e32 v14, v8, v14
	v_add_f32_e32 v15, v13, v15
	v_add_f32_e32 v164, v154, v164
	v_add_f32_e32 v165, v159, v165
	v_add_f32_e32 v14, v2, v14
	v_add_f32_e32 v15, v144, v15
	v_add_f32_e32 v164, v149, v164
	v_add_f32_e32 v165, v160, v165
	v_add_f32_e32 v14, v4, v14
	v_add_f32_e32 v15, v145, v15
	v_add_f32_e32 v164, v151, v164
	v_add_f32_e32 v165, v161, v165
	v_add_f32_e32 v14, v7, v14
	v_add_f32_e32 v15, v146, v15
	v_add_f32_e32 v164, v153, v164
	v_add_f32_e32 v165, v162, v165
	v_add_f32_e32 v14, v9, v14
	v_add_f32_e32 v15, v147, v15
	v_add_f32_e32 v164, v155, v164
	v_add_f32_e32 v165, v163, v165
	v_add_f32_e32 v14, v14, v15
	v_add_f32_e32 v15, v164, v165
	v_add_f32_e32 v14, v14, v15
	v_mov_b32_e32 v15, v14
	v_cvt_pk_bf16_f32 v208, v6, v3
	v_cvt_pk_bf16_f32 v209, v5, v8
	v_cvt_pk_bf16_f32 v210, v10, v11
	v_cvt_pk_bf16_f32 v211, v12, v13
	v_cvt_pk_bf16_f32 v10, v148, v150
	v_cvt_pk_bf16_f32 v11, v152, v154
	v_cvt_pk_bf16_f32 v12, v156, v157
	v_cvt_pk_bf16_f32 v13, v158, v159
	v_cvt_pk_bf16_f32 v6, v2, v4
	v_cvt_pk_bf16_f32 v7, v7, v9
	v_cvt_pk_bf16_f32 v8, v144, v145
	v_cvt_pk_bf16_f32 v9, v146, v147
	v_cvt_pk_bf16_f32 v2, v149, v151
	v_cvt_pk_bf16_f32 v3, v153, v155
	v_cvt_pk_bf16_f32 v4, v160, v161
	v_cvt_pk_bf16_f32 v5, v162, v163
	v_permlane32_swap_b32_e32 v14, v15
	v_permlane32_swap_b32_e32 v208, v210
	v_permlane32_swap_b32_e32 v209, v211
	v_permlane32_swap_b32_e32 v10, v12
	v_permlane32_swap_b32_e32 v11, v13
	v_permlane32_swap_b32_e32 v6, v8
	v_permlane32_swap_b32_e32 v7, v9
	v_permlane32_swap_b32_e32 v2, v4
	v_permlane32_swap_b32_e32 v3, v5
	s_nop 15
	v_mov_b32_e32 v160, 0
	s_andn2_b64 vcc, exec, s[44:45]
	v_mov_b32_e32 v161, 0
	v_mov_b32_e32 v162, 0
	v_mov_b32_e32 v163, 0
	v_mov_b32_e32 v164, 0
	v_mov_b32_e32 v165, 0
	v_mov_b32_e32 v166, 0
	v_mov_b32_e32 v167, 0
	v_mov_b32_e32 v168, 0
	v_mov_b32_e32 v169, 0
	v_mov_b32_e32 v170, 0
	v_mov_b32_e32 v171, 0
	v_mov_b32_e32 v172, 0
	v_mov_b32_e32 v173, 0
	v_mov_b32_e32 v174, 0
	v_mov_b32_e32 v175, 0
	v_mov_b32_e32 v144, 0
	v_mov_b32_e32 v145, 0
	v_mov_b32_e32 v146, 0
	v_mov_b32_e32 v147, 0
	v_mov_b32_e32 v148, 0
	v_mov_b32_e32 v149, 0
	v_mov_b32_e32 v150, 0
	v_mov_b32_e32 v151, 0
	v_mov_b32_e32 v152, 0
	v_mov_b32_e32 v153, 0
	v_mov_b32_e32 v154, 0
	v_mov_b32_e32 v155, 0
	v_mov_b32_e32 v156, 0
	v_mov_b32_e32 v157, 0
	v_mov_b32_e32 v158, 0
	v_mov_b32_e32 v159, 0
	s_cbranch_vccnz .LBB0_200
	s_andn2_b64 vcc, exec, s[42:43]
	s_mov_b64 s[42:43], -1
	s_cbranch_vccnz .LBB0_198
	v_add_u32_e32 v144, 0x21780, v212
	v_add_u32_e32 v146, 0x21708, v212
	v_add_u32_e32 v147, 0x21788, v212
	v_add_u32_e32 v148, 0x21720, v212
	v_add_u32_e32 v149, 0x217a0, v212
	v_add_u32_e32 v150, 0x21728, v212
	v_add_u32_e32 v151, 0x217a8, v212
	v_add_u32_e32 v152, 0x21740, v212
	v_add_u32_e32 v153, 0x217c0, v212
	v_add_u32_e32 v154, 0x21748, v212
	v_add_u32_e32 v155, 0x217c8, v212
	v_add_u32_e32 v156, 0x21760, v212
	v_add_u32_e32 v157, 0x217e0, v212
	v_add_u32_e32 v158, 0x21768, v212
	v_add_u32_e32 v159, 0x217e8, v212
	ds_read2_b32 v[160:161], v213 offset1:1
	ds_read2_b32 v[144:145], v144 offset1:1
	ds_read2_b32 v[162:163], v146 offset1:1
	ds_read2_b32 v[146:147], v147 offset1:1
	ds_read2_b32 v[164:165], v148 offset1:1
	ds_read2_b32 v[148:149], v149 offset1:1
	ds_read2_b32 v[166:167], v150 offset1:1
	ds_read2_b32 v[150:151], v151 offset1:1
	ds_read2_b32 v[168:169], v152 offset1:1
	ds_read2_b32 v[152:153], v153 offset1:1
	ds_read2_b32 v[170:171], v154 offset1:1
	ds_read2_b32 v[154:155], v155 offset1:1
	ds_read2_b32 v[172:173], v156 offset1:1
	ds_read2_b32 v[156:157], v157 offset1:1
	ds_read2_b32 v[174:175], v158 offset1:1
	ds_read2_b32 v[158:159], v159 offset1:1
	s_mov_b64 s[42:43], 0
